# baseline (speedup 1.0000x reference)
_Z14attn_bh_kernelPKDF16_S0_S0_PDF16_i:
	s_load_dwordx4 s[8:11], s[0:1], 0x0
	s_load_dwordx2 s[4:5], s[0:1], 0x10
	s_load_dword s3, s[0:1], 0x20
	v_lshrrev_b32_e32 v2, 6, v0
	v_and_b32_e32 v86, 31, v0
	s_lshr_b32 s6, s2, 3
	s_mul_i32 s12, s6, 0x248
	s_waitcnt lgkmcnt(0)
	v_add_u32_e32 v87, s3, v2
	v_lshl_or_b32 v2, v87, 5, v86
	v_min_i32_e32 v2, 0x247, v2
	v_add_u32_e32 v2, s12, v2
	v_ashrrev_i32_e32 v3, 31, v2
	s_lshl_b32 s3, s2, 6
	v_lshlrev_b64 v[2:3], 10, v[2:3]
	s_and_b32 s14, s3, 0x1c0
	v_bfe_u32 v1, v0, 5, 1
	v_lshl_add_u64 v[2:3], s[8:9], 0, v[2:3]
	s_mov_b32 s7, 0
	s_lshl_b32 s6, s14, 1
	v_mov_b32_e32 v45, 0
	v_lshl_add_u64 v[2:3], v[2:3], 0, s[6:7]
	v_lshlrev_b32_e32 v42, 4, v1
	v_mov_b32_e32 v43, v45
	s_mul_hi_i32 s3, s2, 0x12400
	s_mul_i32 s2, s2, 0x12400
	v_lshl_add_u64 v[2:3], v[2:3], 0, v[42:43]
	s_add_u32 s2, s4, s2
	global_load_dwordx4 v[66:69], v[2:3], off
	global_load_dwordx4 v[70:73], v[2:3], off offset:32
	global_load_dwordx4 v[74:77], v[2:3], off offset:64
	global_load_dwordx4 v[78:81], v[2:3], off offset:96
	s_addc_u32 s3, s5, s3
	s_ashr_i32 s13, s12, 31
	s_lshl_b64 s[16:17], s[12:13], 10
	s_add_u32 s16, s10, s16
	s_addc_u32 s17, s11, s17
	s_add_u32 s16, s16, s6
	s_addc_u32 s17, s17, 0
	v_lshrrev_b32_e32 v4, 6, v0
	v_and_b32_e32 v5, 63, v0
	v_lshrrev_b32_e32 v6, 3, v5
	v_readfirstlane_b32 s15, v4
	v_and_b32_e32 v7, 7, v5
	s_movk_i32 s23, 0x400
	s_movk_i32 s24, 0x490
	s_mov_b32 s19, 0x10000
	s_movk_i32 s20, 0x80
	s_and_b32 s18, s15, 7
	s_lshl_b32 s21, s18, 3
	s_lshl_b32 s18, s18, 10
	v_add_u32_e32 v9, s21, v6
	s_cmp_lt_u32 s15, 8
	s_cselect_b32 s23, s23, s24
	s_cselect_b32 s21, s19, s20
	s_cselect_b32 s16, s16, s2
	s_cselect_b32 s17, s17, s3
	s_cselect_b32 s24, 0, 0x12400
	s_add_u32 s18, s18, s24
	v_bfe_u32 v10, v9, 1, 3
	v_xor_b32_e32 v10, v10, v7
	v_mul_u32_u24_e32 v8, s23, v9
	v_lshl_add_u32 v8, v10, 4, v8
	s_mov_b32 m0, s18
	s_add_u32 s18, s18, 0x2000
	global_load_lds_dwordx4 v8, s[16:17]
	v_add_u32_e32 v8, s21, v8
	s_cmp_lg_u32 s15, 0
	s_cbranch_scc1 .Lat_nw0
	v_add_u32_e32 v11, 0x80000, v8
	s_mov_b32 m0, 0x12000
	s_nop 0
	global_load_lds_dwordx4 v11, s[16:17]

.Lat_nt9:
	v_and_b32_e32 v2, 19, v0
	v_lshlrev_b32_e32 v3, 1, v0
	v_lshrrev_b32_e32 v0, 1, v0
	v_and_b32_e32 v3, 8, v3
	v_and_b32_e32 v0, 4, v0
	v_or3_b32 v0, v3, v2, v0
	v_lshrrev_b32_e32 v2, 1, v0
	v_bfe_u32 v3, v0, 1, 3
	v_lshlrev_b32_e32 v0, 7, v0
	v_bitop3_b32 v2, v1, v2, 7 bitop3:0x78
	v_lshl_add_u32 v88, v2, 4, v0
	v_bitop3_b32 v2, v1, v3, 2 bitop3:0x36
	v_lshl_add_u32 v89, v2, 4, v0
	v_bitop3_b32 v2, v1, v3, 4 bitop3:0x36
	v_lshl_add_u32 v90, v2, 4, v0
	v_bitop3_b32 v2, v1, v3, 6 bitop3:0x36
	v_lshl_add_u32 v91, v2, 4, v0
	v_bfe_u32 v3, v86, 1, 3
	v_lshlrev_b32_e32 v2, 7, v86
	v_add_u32_e32 v2, 0x12400, v2
	v_xor_b32_e32 v4, v1, v3
	v_lshl_add_u32 v93, v4, 4, v2
	v_or_b32_e32 v4, 2, v1
	v_xor_b32_e32 v4, v4, v3
	v_lshl_add_u32 v114, v4, 4, v2
	v_or_b32_e32 v4, 4, v1
	v_xor_b32_e32 v4, v4, v3
	v_lshl_add_u32 v115, v4, 4, v2
	v_or_b32_e32 v4, 6, v1
	v_xor_b32_e32 v4, v4, v3
	v_lshl_add_u32 v116, v4, 4, v2
	s_mov_b32 s22, 1
	v_cmp_gt_i32_e32 vcc, 19, v87
	s_waitcnt lgkmcnt(0)
	s_barrier
	s_mov_b32 m0, s18
	s_add_u32 s18, s18, 0x2000
	global_load_lds_dwordx4 v8, s[16:17]
	v_add_u32_e32 v8, s21, v8
	s_mov_b32 m0, s18
	s_add_u32 s18, s18, 0x2000
	global_load_lds_dwordx4 v8, s[16:17]
	v_add_u32_e32 v8, s21, v8
	s_mov_b32 m0, s18
	s_add_u32 s18, s18, 0x2000
	global_load_lds_dwordx4 v8, s[16:17]
	v_add_u32_e32 v8, s21, v8
	s_mov_b32 m0, s18
	s_add_u32 s18, s18, 0x2000
	global_load_lds_dwordx4 v8, s[16:17]
	v_add_u32_e32 v8, s21, v8
	s_mov_b32 m0, s18
	s_add_u32 s18, s18, 0x2000
	global_load_lds_dwordx4 v8, s[16:17]
	v_add_u32_e32 v8, s21, v8
	s_mov_b32 m0, s18
	s_add_u32 s18, s18, 0x2000
	global_load_lds_dwordx4 v8, s[16:17]
	v_add_u32_e32 v8, s21, v8
	s_mov_b32 m0, s18
	s_add_u32 s18, s18, 0x2000
	global_load_lds_dwordx4 v8, s[16:17]
	v_add_u32_e32 v8, s21, v8
	s_mov_b32 m0, s18
	s_add_u32 s18, s18, 0x2000
	global_load_lds_dwordx4 v8, s[16:17]
	v_add_u32_e32 v8, s21, v8
	s_and_saveexec_b64 s[2:3], vcc
	s_cbranch_execz .Lat_notile
	s_load_dwordx2 s[4:5], s[0:1], 0x18
	v_lshlrev_b32_e32 v92, 3, v1
	s_add_u32 s0, s8, s6
	v_mov_b32_e32 v0, 0
	s_addc_u32 s1, s9, 0
	v_lshlrev_b32_e32 v2, 1, v92
	v_mov_b32_e32 v3, v0
	v_or_b32_e32 v1, s14, v92
	v_lshl_add_u64 v[82:83], s[0:1], 0, v[2:3]
	s_mov_b32 s7, 0x20000
	s_brev_b32 s6, -2
	s_waitcnt lgkmcnt(0)
	s_and_b32 s5, s5, 0xffff
	s_mov_b64 s[2:3], 0
	s_movk_i32 s13, 0x248
	v_mov_b32_e32 v94, 0x247
	s_movk_i32 s18, 0x205
	s_mov_b32 s19, 0x41000000
	s_mov_b32 s20, 0xc1000000
	v_lshlrev_b32_e32 v95, 1, v1
	v_mov_b32_e32 v96, 0xf149f2ca
	v_mov_b32_e32 v97, v87
	s_branch .LBB2_9

.LBB2_14:
	s_cmp_eq_u32 s22, 0
	s_cbranch_scc1 .Lat_qkA
	s_cmp_lg_u32 s21, 0x40
	s_cbranch_scc1 .Lat_qkB
	s_waitcnt vmcnt(0)
	s_barrier
	s_mov_b32 s22, 0
	s_branch .Lat_qkA
